# conv: 8 tokens per step accumulated first, group-norm sums reduced together by a reduce-scatter butterfly (DPP + permlane swaps)
# speedup vs baseline: 1.0121x; 1.0098x over previous
; __device__ __forceinline__ void ph_conv2(const Params& p, int l, LAS unsigned char* lds, const int wvid) {
;     ...
;         for (int tb = 0; tb < (ntok >> 4); ++tb) {
;             const int tl = th * (ntok >> 1) + tb * 8;
;             float x[38];
; #pragma unroll
;             for (int i = 0; i < 38; ++i) x[i] = G[(tl + i) * 256 + c];
; #pragma unroll
;             for (int o = 0; o < 8; ++o) { float acc = cb;
; #pragma unroll
;                 for (int w = 0; w < 31; ++w) acc += wv[w] * x[o + w];
.LBB0_456:
	ds_read2st64_b32 v[40:41], v0 offset1:4
	ds_read2st64_b32 v[38:39], v0 offset0:8 offset1:12
	ds_read2st64_b32 v[36:37], v0 offset0:16 offset1:20
	ds_read2st64_b32 v[34:35], v0 offset0:24 offset1:28
	ds_read2st64_b32 v[32:33], v0 offset0:32 offset1:36
	ds_read2st64_b32 v[30:31], v0 offset0:40 offset1:44
	ds_read2st64_b32 v[28:29], v0 offset0:48 offset1:52
	ds_read2st64_b32 v[26:27], v0 offset0:56 offset1:60
	ds_read2st64_b32 v[24:25], v0 offset0:64 offset1:68
	ds_read2st64_b32 v[22:23], v0 offset0:72 offset1:76
	ds_read2st64_b32 v[20:21], v0 offset0:80 offset1:84
	ds_read2st64_b32 v[18:19], v0 offset0:88 offset1:92
	ds_read2st64_b32 v[16:17], v0 offset0:96 offset1:100
	ds_read2st64_b32 v[14:15], v0 offset0:104 offset1:108
	ds_read2st64_b32 v[12:13], v0 offset0:112 offset1:116
	ds_read2st64_b32 v[10:11], v0 offset0:120 offset1:124
	ds_read2st64_b32 v[8:9], v0 offset0:128 offset1:132
	ds_read2st64_b32 v[6:7], v0 offset0:136 offset1:140
	ds_read2st64_b32 v[4:5], v0 offset0:144 offset1:148
	s_waitcnt lgkmcnt(15)
	v_fma_f32 v120, v60, v40, v55
	v_fmac_f32_e32 v120, v61, v41
	s_waitcnt lgkmcnt(15)
	v_fmac_f32_e32 v120, v62, v38
	v_fmac_f32_e32 v120, v63, v39
	s_waitcnt lgkmcnt(15)
	v_fmac_f32_e32 v120, v64, v36
	v_fmac_f32_e32 v120, v65, v37
	s_waitcnt lgkmcnt(15)
	v_fmac_f32_e32 v120, v66, v34
	v_fmac_f32_e32 v120, v67, v35
	s_waitcnt lgkmcnt(14)
	v_fmac_f32_e32 v120, v68, v32
	v_fmac_f32_e32 v120, v69, v33
	s_waitcnt lgkmcnt(13)
	v_fmac_f32_e32 v120, v70, v30
	v_fmac_f32_e32 v120, v71, v31
	s_waitcnt lgkmcnt(12)
	v_fmac_f32_e32 v120, v72, v28
	v_fmac_f32_e32 v120, v73, v29
	s_waitcnt lgkmcnt(11)
	v_fmac_f32_e32 v120, v74, v26
	v_fmac_f32_e32 v120, v75, v27
	s_waitcnt lgkmcnt(10)
	v_fmac_f32_e32 v120, v76, v24
	v_fmac_f32_e32 v120, v77, v25
	s_waitcnt lgkmcnt(9)
	v_fmac_f32_e32 v120, v78, v22
	v_fmac_f32_e32 v120, v79, v23
	s_waitcnt lgkmcnt(8)
	v_fmac_f32_e32 v120, v80, v20
	v_fmac_f32_e32 v120, v81, v21
	s_waitcnt lgkmcnt(7)
	v_fmac_f32_e32 v120, v82, v18
	v_fmac_f32_e32 v120, v83, v19
	s_waitcnt lgkmcnt(6)
	v_fmac_f32_e32 v120, v84, v16
	v_fmac_f32_e32 v120, v85, v17
	s_waitcnt lgkmcnt(5)
	v_fmac_f32_e32 v120, v86, v14
	v_fmac_f32_e32 v120, v87, v15
	s_waitcnt lgkmcnt(4)
	v_fmac_f32_e32 v120, v88, v12
	v_fmac_f32_e32 v120, v89, v13
	s_waitcnt lgkmcnt(3)
	v_fmac_f32_e32 v120, v90, v10
	v_fma_f32 v121, v60, v41, v55
	v_fmac_f32_e32 v121, v61, v38
	v_fmac_f32_e32 v121, v62, v39
	v_fmac_f32_e32 v121, v63, v36
	v_fmac_f32_e32 v121, v64, v37
	v_fmac_f32_e32 v121, v65, v34
	v_fmac_f32_e32 v121, v66, v35
	v_fmac_f32_e32 v121, v67, v32
	v_fmac_f32_e32 v121, v68, v33
	v_fmac_f32_e32 v121, v69, v30
	v_fmac_f32_e32 v121, v70, v31
	v_fmac_f32_e32 v121, v71, v28
	v_fmac_f32_e32 v121, v72, v29
	v_fmac_f32_e32 v121, v73, v26
	v_fmac_f32_e32 v121, v74, v27
	v_fmac_f32_e32 v121, v75, v24
	v_fmac_f32_e32 v121, v76, v25
	v_fmac_f32_e32 v121, v77, v22
	v_fmac_f32_e32 v121, v78, v23
	v_fmac_f32_e32 v121, v79, v20
	v_fmac_f32_e32 v121, v80, v21
	v_fmac_f32_e32 v121, v81, v18
	v_fmac_f32_e32 v121, v82, v19
	v_fmac_f32_e32 v121, v83, v16
	v_fmac_f32_e32 v121, v84, v17
	v_fmac_f32_e32 v121, v85, v14
	v_fmac_f32_e32 v121, v86, v15
	v_fmac_f32_e32 v121, v87, v12
	v_fmac_f32_e32 v121, v88, v13
	v_fmac_f32_e32 v121, v89, v10
	v_fmac_f32_e32 v121, v90, v11
	v_fma_f32 v122, v60, v38, v55
	v_fmac_f32_e32 v122, v61, v39
	v_fmac_f32_e32 v122, v62, v36
	v_fmac_f32_e32 v122, v63, v37
	v_fmac_f32_e32 v122, v64, v34
	v_fmac_f32_e32 v122, v65, v35
	v_fmac_f32_e32 v122, v66, v32
	v_fmac_f32_e32 v122, v67, v33
	v_fmac_f32_e32 v122, v68, v30
	v_fmac_f32_e32 v122, v69, v31
	v_fmac_f32_e32 v122, v70, v28
	v_fmac_f32_e32 v122, v71, v29
	v_fmac_f32_e32 v122, v72, v26
	v_fmac_f32_e32 v122, v73, v27
	v_fmac_f32_e32 v122, v74, v24
	v_fmac_f32_e32 v122, v75, v25
	v_fmac_f32_e32 v122, v76, v22
	v_fmac_f32_e32 v122, v77, v23
	v_fmac_f32_e32 v122, v78, v20
	v_fmac_f32_e32 v122, v79, v21
	v_fmac_f32_e32 v122, v80, v18
	v_fmac_f32_e32 v122, v81, v19
	v_fmac_f32_e32 v122, v82, v16
	v_fmac_f32_e32 v122, v83, v17
	v_fmac_f32_e32 v122, v84, v14
	v_fmac_f32_e32 v122, v85, v15
	v_fmac_f32_e32 v122, v86, v12
	v_fmac_f32_e32 v122, v87, v13
	v_fmac_f32_e32 v122, v88, v10
	v_fmac_f32_e32 v122, v89, v11
	s_waitcnt lgkmcnt(2)
	v_fmac_f32_e32 v122, v90, v8
	v_fma_f32 v123, v60, v39, v55
	v_fmac_f32_e32 v123, v61, v36
	v_fmac_f32_e32 v123, v62, v37
	v_fmac_f32_e32 v123, v63, v34
	v_fmac_f32_e32 v123, v64, v35
	v_fmac_f32_e32 v123, v65, v32
	v_fmac_f32_e32 v123, v66, v33
	v_fmac_f32_e32 v123, v67, v30
	v_fmac_f32_e32 v123, v68, v31
	v_fmac_f32_e32 v123, v69, v28
	v_fmac_f32_e32 v123, v70, v29
	v_fmac_f32_e32 v123, v71, v26
	v_fmac_f32_e32 v123, v72, v27
	v_fmac_f32_e32 v123, v73, v24
	v_fmac_f32_e32 v123, v74, v25
	v_fmac_f32_e32 v123, v75, v22
	v_fmac_f32_e32 v123, v76, v23
	v_fmac_f32_e32 v123, v77, v20
	v_fmac_f32_e32 v123, v78, v21
	v_fmac_f32_e32 v123, v79, v18
	v_fmac_f32_e32 v123, v80, v19
	v_fmac_f32_e32 v123, v81, v16
	v_fmac_f32_e32 v123, v82, v17
	v_fmac_f32_e32 v123, v83, v14
	v_fmac_f32_e32 v123, v84, v15
	v_fmac_f32_e32 v123, v85, v12
	v_fmac_f32_e32 v123, v86, v13
	v_fmac_f32_e32 v123, v87, v10
	v_fmac_f32_e32 v123, v88, v11
	v_fmac_f32_e32 v123, v89, v8
	v_fmac_f32_e32 v123, v90, v9
	v_fma_f32 v124, v60, v36, v55
	v_fmac_f32_e32 v124, v61, v37
	v_fmac_f32_e32 v124, v62, v34
	v_fmac_f32_e32 v124, v63, v35
	v_fmac_f32_e32 v124, v64, v32
	v_fmac_f32_e32 v124, v65, v33
	v_fmac_f32_e32 v124, v66, v30
	v_fmac_f32_e32 v124, v67, v31
	v_fmac_f32_e32 v124, v68, v28
	v_fmac_f32_e32 v124, v69, v29
	v_fmac_f32_e32 v124, v70, v26
	v_fmac_f32_e32 v124, v71, v27
	v_fmac_f32_e32 v124, v72, v24
	v_fmac_f32_e32 v124, v73, v25
	v_fmac_f32_e32 v124, v74, v22
	v_fmac_f32_e32 v124, v75, v23
	v_fmac_f32_e32 v124, v76, v20
	v_fmac_f32_e32 v124, v77, v21
	v_fmac_f32_e32 v124, v78, v18
	v_fmac_f32_e32 v124, v79, v19
	v_fmac_f32_e32 v124, v80, v16
	v_fmac_f32_e32 v124, v81, v17
	v_fmac_f32_e32 v124, v82, v14
	v_fmac_f32_e32 v124, v83, v15
	v_fmac_f32_e32 v124, v84, v12
	v_fmac_f32_e32 v124, v85, v13
	v_fmac_f32_e32 v124, v86, v10
	v_fmac_f32_e32 v124, v87, v11
	v_fmac_f32_e32 v124, v88, v8
	v_fmac_f32_e32 v124, v89, v9
	s_waitcnt lgkmcnt(1)
; __device__ __forceinline__ float frsq(float x) { return __builtin_amdgcn_rsqf(x); }
; __device__ __forceinline__ float row_sum16(float v) {
;     v = dpp_add<0xB1, 0xF>(v); v = dpp_add<0x4E, 0xF>(v); v = dpp_add<0x141, 0xF>(v); v = dpp_add<0x140, 0xF>(v); return v;
; }
; __device__ __forceinline__ float wave_sum(float v) {
;     v = row_sum16(v); v = dpp_add<0x142, 0xA>(v); v = dpp_add<0x143, 0xC>(v);
;     return __int_as_float(__builtin_amdgcn_readlane(__float_as_int(v), 63));
; __device__ __forceinline__ void ph_conv2(const Params& p, int l, LAS unsigned char* lds, const int wvid) {
;     ...
;             for (int o = 0; o < 8; ++o) { float acc = cb;
; #pragma unroll
;                 for (int w = 0; w < 31; ++w) acc += wv[w] * x[o + w];
;                 const float mean = wave_sum(acc) * (1.f / 64.f); const float dv = acc - mean; const float var = wave_sum(dv * dv) * (1.f / 64.f);
;                 const float y = dv * frsq(var + 1e-5f) * gg + gb;
	v_fmac_f32_e32 v124, v90, v6
	v_fma_f32 v125, v60, v37, v55
	v_fmac_f32_e32 v125, v61, v34
	v_fmac_f32_e32 v125, v62, v35
	v_fmac_f32_e32 v125, v63, v32
	v_fmac_f32_e32 v125, v64, v33
	v_fmac_f32_e32 v125, v65, v30
	v_fmac_f32_e32 v125, v66, v31
	v_fmac_f32_e32 v125, v67, v28
	v_fmac_f32_e32 v125, v68, v29
	v_fmac_f32_e32 v125, v69, v26
	v_fmac_f32_e32 v125, v70, v27
	v_fmac_f32_e32 v125, v71, v24
	v_fmac_f32_e32 v125, v72, v25
	v_fmac_f32_e32 v125, v73, v22
	v_fmac_f32_e32 v125, v74, v23
	v_fmac_f32_e32 v125, v75, v20
	v_fmac_f32_e32 v125, v76, v21
	v_fmac_f32_e32 v125, v77, v18
	v_fmac_f32_e32 v125, v78, v19
	v_fmac_f32_e32 v125, v79, v16
	v_fmac_f32_e32 v125, v80, v17
	v_fmac_f32_e32 v125, v81, v14
	v_fmac_f32_e32 v125, v82, v15
	v_fmac_f32_e32 v125, v83, v12
	v_fmac_f32_e32 v125, v84, v13
	v_fmac_f32_e32 v125, v85, v10
	v_fmac_f32_e32 v125, v86, v11
	v_fmac_f32_e32 v125, v87, v8
	v_fmac_f32_e32 v125, v88, v9
	v_fmac_f32_e32 v125, v89, v6
	v_fmac_f32_e32 v125, v90, v7
	v_fma_f32 v126, v60, v34, v55
	v_fmac_f32_e32 v126, v61, v35
	v_fmac_f32_e32 v126, v62, v32
	v_fmac_f32_e32 v126, v63, v33
	v_fmac_f32_e32 v126, v64, v30
	v_fmac_f32_e32 v126, v65, v31
	v_fmac_f32_e32 v126, v66, v28
	v_fmac_f32_e32 v126, v67, v29
	v_fmac_f32_e32 v126, v68, v26
	v_fmac_f32_e32 v126, v69, v27
	v_fmac_f32_e32 v126, v70, v24
	v_fmac_f32_e32 v126, v71, v25
	v_fmac_f32_e32 v126, v72, v22
	v_fmac_f32_e32 v126, v73, v23
	v_fmac_f32_e32 v126, v74, v20
	v_fmac_f32_e32 v126, v75, v21
	v_fmac_f32_e32 v126, v76, v18
	v_fmac_f32_e32 v126, v77, v19
	v_fmac_f32_e32 v126, v78, v16
	v_fmac_f32_e32 v126, v79, v17
	v_fmac_f32_e32 v126, v80, v14
	v_fmac_f32_e32 v126, v81, v15
	v_fmac_f32_e32 v126, v82, v12
	v_fmac_f32_e32 v126, v83, v13
	v_fmac_f32_e32 v126, v84, v10
	v_fmac_f32_e32 v126, v85, v11
	v_fmac_f32_e32 v126, v86, v8
	v_fmac_f32_e32 v126, v87, v9
	v_fmac_f32_e32 v126, v88, v6
	v_fmac_f32_e32 v126, v89, v7
	s_waitcnt lgkmcnt(0)
	v_fmac_f32_e32 v126, v90, v4
	v_fma_f32 v127, v60, v35, v55
	v_fmac_f32_e32 v127, v61, v32
	v_fmac_f32_e32 v127, v62, v33
	v_fmac_f32_e32 v127, v63, v30
	v_fmac_f32_e32 v127, v64, v31
	v_fmac_f32_e32 v127, v65, v28
	v_fmac_f32_e32 v127, v66, v29
	v_fmac_f32_e32 v127, v67, v26
	v_fmac_f32_e32 v127, v68, v27
	v_fmac_f32_e32 v127, v69, v24
	v_fmac_f32_e32 v127, v70, v25
	v_fmac_f32_e32 v127, v71, v22
	v_fmac_f32_e32 v127, v72, v23
	v_fmac_f32_e32 v127, v73, v20
	v_fmac_f32_e32 v127, v74, v21
	v_fmac_f32_e32 v127, v75, v18
	v_fmac_f32_e32 v127, v76, v19
	v_fmac_f32_e32 v127, v77, v16
	v_fmac_f32_e32 v127, v78, v17
	v_fmac_f32_e32 v127, v79, v14
	v_fmac_f32_e32 v127, v80, v15
	v_fmac_f32_e32 v127, v81, v12
	v_fmac_f32_e32 v127, v82, v13
	v_fmac_f32_e32 v127, v83, v10
	v_fmac_f32_e32 v127, v84, v11
	v_fmac_f32_e32 v127, v85, v8
	v_fmac_f32_e32 v127, v86, v9
	v_fmac_f32_e32 v127, v87, v6
	v_fmac_f32_e32 v127, v88, v7
	v_fmac_f32_e32 v127, v89, v4
	v_fmac_f32_e32 v127, v90, v5
	s_mov_b32 vcc_lo, 0x5a5a5a5a
	s_mov_b32 vcc_hi, 0x5a5a5a5a
	v_cndmask_b32_e32 v136, v121, v120, vcc
	v_cndmask_b32_e32 v137, v123, v122, vcc
	v_cndmask_b32_e32 v138, v125, v124, vcc
	v_cndmask_b32_e32 v139, v127, v126, vcc
	v_cndmask_b32_e32 v140, v120, v121, vcc
	v_cndmask_b32_e32 v141, v122, v123, vcc
	v_cndmask_b32_e32 v142, v124, v125, vcc
	v_cndmask_b32_e32 v143, v126, v127, vcc
	v_add_f32_dpp v144, v136, v140 quad_perm:[1,0,3,2] row_mask:0xf bank_mask:0xf
	v_add_f32_dpp v145, v137, v141 quad_perm:[1,0,3,2] row_mask:0xf bank_mask:0xf
	v_add_f32_dpp v146, v138, v142 quad_perm:[1,0,3,2] row_mask:0xf bank_mask:0xf
	v_add_f32_dpp v147, v139, v143 quad_perm:[1,0,3,2] row_mask:0xf bank_mask:0xf
	s_mov_b32 vcc_lo, 0x3c3c3c3c
	s_mov_b32 vcc_hi, 0x3c3c3c3c
	v_cndmask_b32_e32 v148, v145, v144, vcc
	v_cndmask_b32_e32 v149, v147, v146, vcc
	v_cndmask_b32_e32 v150, v144, v145, vcc
	v_cndmask_b32_e32 v151, v146, v147, vcc
	s_nop 0
	v_add_f32_dpp v136, v148, v150 quad_perm:[2,3,0,1] row_mask:0xf bank_mask:0xf
	v_add_f32_dpp v137, v149, v151 quad_perm:[2,3,0,1] row_mask:0xf bank_mask:0xf
	s_mov_b32 vcc_lo, 0xff00ff00
	s_mov_b32 vcc_hi, 0xff00ff00
	v_cndmask_b32_e32 v138, v137, v136, vcc
	v_cndmask_b32_e32 v139, v136, v137, vcc
	s_nop 1
	v_add_f32_dpp v140, v138, v139 row_ror:8 row_mask:0xf bank_mask:0xf
	s_nop 1
	v_add_f32_dpp v141, v140, v140 row_half_mirror row_mask:0xf bank_mask:0xf
	v_mov_b32_e32 v142, v141
	s_nop 1
	v_permlane16_swap_b32_e32 v141, v142
	v_add_f32_e32 v143, v141, v142
	v_mov_b32_e32 v144, v143
	s_nop 1
	v_permlane32_swap_b32_e32 v143, v144
	v_add_f32_e32 v145, v143, v144
	s_nop 0
	v_readlane_b32 s24, v145, 0
	v_readlane_b32 s25, v145, 1
	v_readlane_b32 s26, v145, 2
	v_readlane_b32 s27, v145, 3
	v_readlane_b32 s28, v145, 8
	v_readlane_b32 s29, v145, 9
	v_readlane_b32 s30, v145, 10
	v_readlane_b32 s31, v145, 11
	v_fmac_f32_e32 v120, s24, v214
	v_fmac_f32_e32 v121, s25, v214
	v_fmac_f32_e32 v122, s26, v214
	v_fmac_f32_e32 v123, s27, v214
	v_fmac_f32_e32 v124, s28, v214
	v_fmac_f32_e32 v125, s29, v214
	v_fmac_f32_e32 v126, s30, v214
	v_fmac_f32_e32 v127, s31, v214
	v_mul_f32_e32 v128, v120, v120
	v_mul_f32_e32 v129, v121, v121
	v_mul_f32_e32 v130, v122, v122
	v_mul_f32_e32 v131, v123, v123
	v_mul_f32_e32 v132, v124, v124
	v_mul_f32_e32 v133, v125, v125
	v_mul_f32_e32 v134, v126, v126
	v_mul_f32_e32 v135, v127, v127
	s_mov_b32 vcc_lo, 0x5a5a5a5a
	s_mov_b32 vcc_hi, 0x5a5a5a5a
	v_cndmask_b32_e32 v136, v129, v128, vcc
	v_cndmask_b32_e32 v137, v131, v130, vcc
	v_cndmask_b32_e32 v138, v133, v132, vcc
	v_cndmask_b32_e32 v139, v135, v134, vcc
	v_cndmask_b32_e32 v140, v128, v129, vcc
	v_cndmask_b32_e32 v141, v130, v131, vcc
	v_cndmask_b32_e32 v142, v132, v133, vcc
; __device__ __forceinline__ bf16_t f2bf(float f) { unsigned u = __float_as_uint(f); u += 0x7FFFu + ((u >> 16) & 1u); return (bf16_t)(u >> 16); }
; __device__ __forceinline__ float frsq(float x) { return __builtin_amdgcn_rsqf(x); }
; __device__ __forceinline__ float sigmoidf_(float x) { return frcp(1.0f + __expf(-x)); }
; __device__ __forceinline__ void ph_conv2(const Params& p, int l, LAS unsigned char* lds, const int wvid) {
;     ...
;             for (int o = 0; o < 8; ++o) { float acc = cb;
; #pragma unroll
;                 for (int w = 0; w < 31; ++w) acc += wv[w] * x[o + w];
;                 const float mean = wave_sum(acc) * (1.f / 64.f); const float dv = acc - mean; const float var = wave_sum(dv * dv) * (1.f / 64.f);
;                 const float y = dv * frsq(var + 1e-5f) * gg + gb;
;                 const int tg = t0 + tl + o;
;                 if (tg < LT) MIX[((size_t)b * LT + tg) * D + M_D + c] = f2bf(y * sigmoidf_(y)); }
	v_cndmask_b32_e32 v143, v134, v135, vcc
	v_add_f32_dpp v144, v136, v140 quad_perm:[1,0,3,2] row_mask:0xf bank_mask:0xf
	v_add_f32_dpp v145, v137, v141 quad_perm:[1,0,3,2] row_mask:0xf bank_mask:0xf
	v_add_f32_dpp v146, v138, v142 quad_perm:[1,0,3,2] row_mask:0xf bank_mask:0xf
	v_add_f32_dpp v147, v139, v143 quad_perm:[1,0,3,2] row_mask:0xf bank_mask:0xf
	s_mov_b32 vcc_lo, 0x3c3c3c3c
	s_mov_b32 vcc_hi, 0x3c3c3c3c
	v_cndmask_b32_e32 v148, v145, v144, vcc
	v_cndmask_b32_e32 v149, v147, v146, vcc
	v_cndmask_b32_e32 v150, v144, v145, vcc
	v_cndmask_b32_e32 v151, v146, v147, vcc
	s_nop 0
	v_add_f32_dpp v136, v148, v150 quad_perm:[2,3,0,1] row_mask:0xf bank_mask:0xf
	v_add_f32_dpp v137, v149, v151 quad_perm:[2,3,0,1] row_mask:0xf bank_mask:0xf
	s_mov_b32 vcc_lo, 0xff00ff00
	s_mov_b32 vcc_hi, 0xff00ff00
	v_cndmask_b32_e32 v138, v137, v136, vcc
	v_cndmask_b32_e32 v139, v136, v137, vcc
	s_nop 1
	v_add_f32_dpp v140, v138, v139 row_ror:8 row_mask:0xf bank_mask:0xf
	s_nop 1
	v_add_f32_dpp v141, v140, v140 row_half_mirror row_mask:0xf bank_mask:0xf
	v_mov_b32_e32 v142, v141
	s_nop 1
	v_permlane16_swap_b32_e32 v141, v142
	v_add_f32_e32 v143, v141, v142
	v_mov_b32_e32 v144, v143
	s_nop 1
	v_permlane32_swap_b32_e32 v143, v144
	v_add_f32_e32 v145, v143, v144
	s_nop 0
	v_readlane_b32 s24, v145, 0
	v_readlane_b32 s25, v145, 1
	v_readlane_b32 s26, v145, 2
	v_readlane_b32 s27, v145, 3
	v_readlane_b32 s28, v145, 8
	v_readlane_b32 s29, v145, 9
	v_readlane_b32 s30, v145, 10
	v_readlane_b32 s31, v145, 11
	v_fma_f32 v128, s24, v215, v204
	v_fma_f32 v129, s25, v215, v204
	v_fma_f32 v130, s26, v215, v204
	v_fma_f32 v131, s27, v215, v204
	v_fma_f32 v132, s28, v215, v204
	v_fma_f32 v133, s29, v215, v204
	v_fma_f32 v134, s30, v215, v204
	v_fma_f32 v135, s31, v215, v204
	v_rsq_f32_e32 v128, v128
	v_rsq_f32_e32 v129, v129
	v_rsq_f32_e32 v130, v130
	v_rsq_f32_e32 v131, v131
	v_rsq_f32_e32 v132, v132
	v_rsq_f32_e32 v133, v133
	v_rsq_f32_e32 v134, v134
	v_rsq_f32_e32 v135, v135
	v_mul_f32_e32 v120, v120, v128
	v_mul_f32_e32 v121, v121, v129
	v_mul_f32_e32 v122, v122, v130
	v_mul_f32_e32 v123, v123, v131
	v_mul_f32_e32 v124, v124, v132
	v_mul_f32_e32 v125, v125, v133
	v_mul_f32_e32 v126, v126, v134
	v_mul_f32_e32 v127, v127, v135
	v_fma_f32 v120, v58, v120, v59
	v_fma_f32 v121, v58, v121, v59
	v_fma_f32 v122, v58, v122, v59
	v_fma_f32 v123, v58, v123, v59
	v_fma_f32 v124, v58, v124, v59
	v_fma_f32 v125, v58, v125, v59
	v_fma_f32 v126, v58, v126, v59
	v_fma_f32 v127, v58, v127, v59
	v_mul_f32_e32 v128, 0xbfb8aa3b, v120
	v_mul_f32_e32 v129, 0xbfb8aa3b, v121
	v_mul_f32_e32 v130, 0xbfb8aa3b, v122
	v_mul_f32_e32 v131, 0xbfb8aa3b, v123
	v_mul_f32_e32 v132, 0xbfb8aa3b, v124
	v_mul_f32_e32 v133, 0xbfb8aa3b, v125
	v_mul_f32_e32 v134, 0xbfb8aa3b, v126
	v_mul_f32_e32 v135, 0xbfb8aa3b, v127
	v_exp_f32_e32 v128, v128
	v_exp_f32_e32 v129, v129
	v_exp_f32_e32 v130, v130
	v_exp_f32_e32 v131, v131
	v_exp_f32_e32 v132, v132
	v_exp_f32_e32 v133, v133
	v_exp_f32_e32 v134, v134
	v_exp_f32_e32 v135, v135
	v_add_f32_e32 v128, 1.0, v128
	v_add_f32_e32 v129, 1.0, v129
	v_add_f32_e32 v130, 1.0, v130
	v_add_f32_e32 v131, 1.0, v131
	v_add_f32_e32 v132, 1.0, v132
	v_add_f32_e32 v133, 1.0, v133
	v_add_f32_e32 v134, 1.0, v134
	v_add_f32_e32 v135, 1.0, v135
	v_rcp_f32_e32 v128, v128
	v_rcp_f32_e32 v129, v129
	v_rcp_f32_e32 v130, v130
	v_rcp_f32_e32 v131, v131
	v_rcp_f32_e32 v132, v132
	v_rcp_f32_e32 v133, v133
	v_rcp_f32_e32 v134, v134
	v_rcp_f32_e32 v135, v135
	v_mul_f32_e32 v120, v120, v128
	v_mul_f32_e32 v121, v121, v129
	v_mul_f32_e32 v122, v122, v130
	v_mul_f32_e32 v123, v123, v131
	v_mul_f32_e32 v124, v124, v132
	v_mul_f32_e32 v125, v125, v133
	v_mul_f32_e32 v126, v126, v134
	v_mul_f32_e32 v127, v127, v135
	v_bfe_u32 v128, v120, 16, 1
	v_bfe_u32 v129, v121, 16, 1
	v_bfe_u32 v130, v122, 16, 1
	v_bfe_u32 v131, v123, 16, 1
	v_bfe_u32 v132, v124, 16, 1
	v_bfe_u32 v133, v125, 16, 1
	v_bfe_u32 v134, v126, 16, 1
	v_bfe_u32 v135, v127, 16, 1
	v_add3_u32 v120, v120, v128, s79
	v_add3_u32 v121, v121, v129, s79
	v_add3_u32 v122, v122, v130, s79
	v_add3_u32 v123, v123, v131, s79
	v_add3_u32 v124, v124, v132, s79
	v_add3_u32 v125, v125, v133, s79
	v_add3_u32 v126, v126, v134, s79
	v_add3_u32 v127, v127, v135, s79
	v_mov_b32_e32 v4, v2
	v_cmp_gt_i32_e32 vcc, s33, v4
	s_and_saveexec_b64 s[8:9], vcc
	s_cbranch_execz .Lcv_st0
	v_ashrrev_i32_e32 v5, 31, v4
	v_lshl_add_u64 v[4:5], s[6:7], 0, v[4:5]
	v_lshlrev_b64 v[4:5], 11, v[4:5]
	v_lshl_add_u64 v[4:5], v[56:57], 0, v[4:5]
	global_store_short_d16_hi v[4:5], v120, off
.Lcv_st0:
	s_or_b64 exec, exec, s[8:9]
	v_add_u32_e32 v4, 1, v2
	v_cmp_gt_i32_e32 vcc, s33, v4
	s_and_saveexec_b64 s[8:9], vcc
	s_cbranch_execz .Lcv_st1
	v_ashrrev_i32_e32 v5, 31, v4
	v_lshl_add_u64 v[4:5], s[6:7], 0, v[4:5]
	v_lshlrev_b64 v[4:5], 11, v[4:5]
	v_lshl_add_u64 v[4:5], v[56:57], 0, v[4:5]
	global_store_short_d16_hi v[4:5], v121, off
.Lcv_st1:
	s_or_b64 exec, exec, s[8:9]
	v_add_u32_e32 v4, 2, v2
	v_cmp_gt_i32_e32 vcc, s33, v4
	s_and_saveexec_b64 s[8:9], vcc
	s_cbranch_execz .Lcv_st2
	v_ashrrev_i32_e32 v5, 31, v4
	v_lshl_add_u64 v[4:5], s[6:7], 0, v[4:5]
	v_lshlrev_b64 v[4:5], 11, v[4:5]
	v_lshl_add_u64 v[4:5], v[56:57], 0, v[4:5]
	global_store_short_d16_hi v[4:5], v122, off
.Lcv_st2:
	s_or_b64 exec, exec, s[8:9]
	v_add_u32_e32 v4, 3, v2
	v_cmp_gt_i32_e32 vcc, s33, v4
	s_and_saveexec_b64 s[8:9], vcc
	s_cbranch_execz .Lcv_st3
	v_ashrrev_i32_e32 v5, 31, v4
	v_lshl_add_u64 v[4:5], s[6:7], 0, v[4:5]
	v_lshlrev_b64 v[4:5], 11, v[4:5]
	v_lshl_add_u64 v[4:5], v[56:57], 0, v[4:5]
	global_store_short_d16_hi v[4:5], v123, off
.Lcv_st3:
	s_or_b64 exec, exec, s[8:9]
	v_add_u32_e32 v4, 4, v2
	v_cmp_gt_i32_e32 vcc, s33, v4
	s_and_saveexec_b64 s[8:9], vcc
	s_cbranch_execz .Lcv_st4
	v_ashrrev_i32_e32 v5, 31, v4
	v_lshl_add_u64 v[4:5], s[6:7], 0, v[4:5]
	v_lshlrev_b64 v[4:5], 11, v[4:5]
	v_lshl_add_u64 v[4:5], v[56:57], 0, v[4:5]
	global_store_short_d16_hi v[4:5], v124, off
.Lcv_st4:
	s_or_b64 exec, exec, s[8:9]
	v_add_u32_e32 v4, 5, v2
	v_cmp_gt_i32_e32 vcc, s33, v4
	s_and_saveexec_b64 s[8:9], vcc
	s_cbranch_execz .Lcv_st5
	v_ashrrev_i32_e32 v5, 31, v4
	v_lshl_add_u64 v[4:5], s[6:7], 0, v[4:5]
	v_lshlrev_b64 v[4:5], 11, v[4:5]
	v_lshl_add_u64 v[4:5], v[56:57], 0, v[4:5]
	global_store_short_d16_hi v[4:5], v125, off
.Lcv_st5:
	s_or_b64 exec, exec, s[8:9]
	v_add_u32_e32 v4, 6, v2
	v_cmp_gt_i32_e32 vcc, s33, v4
	s_and_saveexec_b64 s[8:9], vcc
	s_cbranch_execz .Lcv_st6
	v_ashrrev_i32_e32 v5, 31, v4
	v_lshl_add_u64 v[4:5], s[6:7], 0, v[4:5]
	v_lshlrev_b64 v[4:5], 11, v[4:5]
	v_lshl_add_u64 v[4:5], v[56:57], 0, v[4:5]
	global_store_short_d16_hi v[4:5], v126, off
.Lcv_st6:
	s_or_b64 exec, exec, s[8:9]
	v_add_u32_e32 v4, 7, v2
	v_cmp_gt_i32_e32 vcc, s33, v4
	s_and_saveexec_b64 s[8:9], vcc
	s_cbranch_execz .Lcv_st7
	v_ashrrev_i32_e32 v5, 31, v4
	v_lshl_add_u64 v[4:5], s[6:7], 0, v[4:5]
	v_lshlrev_b64 v[4:5], 11, v[4:5]
	v_lshl_add_u64 v[4:5], v[56:57], 0, v[4:5]
	global_store_short_d16_hi v[4:5], v127, off
.Lcv_st7:
	s_branch .LBB0_455
